# proj Q/K epilogue tail: emax wave reduction via DPP+readlane instead of six ds_bpermute round trips; redundant sum(va) butterfly kept only in workgroups 0-7
# baseline (speedup 1.0000x reference)
_Z11proj_kernelPKfS0_S0_S0_S0_S0_S0_S0_S0_S0_S0_S0_S0_PfS1_PDF16_S1_S0_S0_S2_:
	s_mov_b32 s88, s2
	s_load_dwordx2 s[16:17], s[0:1], 0x90
	s_load_dwordx4 s[4:7], s[0:1], 0x80
	s_cmpk_gt_u32 s2, 0x5f
	s_mov_b64 s[8:9], -1
	s_cbranch_scc0 .LBB0_16
	s_load_dwordx4 s[8:11], s[0:1], 0x58
	s_lshr_b32 s3, s2, 3
	s_cmpk_gt_u32 s2, 0xbf
	s_mov_b64 s[12:13], -1
	s_cbranch_scc0 .LBB0_3
	v_lshlrev_b32_e32 v54, 2, v0
	v_mov_b32_e32 v55, 0
	s_waitcnt lgkmcnt(0)
	v_lshl_add_u64 v[2:3], s[6:7], 0, v[54:55]
	v_lshl_add_u64 v[4:5], s[16:17], 0, v[54:55]
	v_cmp_gt_u32_e32 vcc, 64, v0
	s_load_dwordx4 s[12:15], s[0:1], 0x38
	s_load_dwordx2 s[22:23], s[0:1], 0x10
	v_cndmask_b32_e32 v2, v4, v2, vcc
	v_cndmask_b32_e32 v3, v5, v3, vcc
	global_load_dword v70, v[2:3], off
	v_lshrrev_b32_e32 v2, 2, v0
	v_and_b32_e32 v56, 15, v0
	v_and_b32_e32 v18, 48, v2
	v_or_b32_e32 v68, v18, v56
	v_bfe_u32 v1, v0, 4, 2
	v_lshlrev_b32_e32 v2, 8, v68
	v_mov_b32_e32 v3, v55
	s_lshl_b32 s20, s2, 1
	v_lshl_add_u64 v[2:3], s[8:9], 0, v[2:3]
	v_lshlrev_b32_e32 v4, 5, v1
	v_mov_b32_e32 v5, v55
	s_and_b32 s20, s20, 6
	s_bfe_u32 s21, s2, 0x10003
	v_lshl_add_u64 v[14:15], v[2:3], 0, v[4:5]
	s_sub_i32 s19, s3, 24
	s_or_b32 s21, s21, s20
	v_lshl_add_u64 v[6:7], v[14:15], 0, 16
	s_mov_b64 s[24:25], 0x80
	s_bfe_u32 s18, s2, 0x10002
	s_lshr_b32 s19, s19, 1
	s_lshl_b32 s20, s21, 6
	v_lshl_add_u64 v[10:11], v[14:15], 0, s[24:25]
	s_mov_b64 s[24:25], 0x90
	v_lshlrev_b32_e32 v22, 2, v18
	v_mov_b32_e32 v23, v55
	s_lshl_b32 s21, s21, 8
	v_lshl_add_u64 v[14:15], v[14:15], 0, s[24:25]
	v_lshl_add_u64 v[24:25], s[10:11], 0, v[22:23]
	v_lshlrev_b32_e32 v18, 4, v1
	v_mov_b32_e32 v19, v55
	s_waitcnt lgkmcnt(0)
	s_add_u32 s14, s14, s21
	v_lshl_add_u64 v[18:19], v[24:25], 0, v[18:19]
	s_addc_u32 s15, s15, 0
	v_lshlrev_b32_e32 v26, 2, v56
	v_mov_b32_e32 v27, v55
	v_lshl_add_u64 v[22:23], s[14:15], 0, v[22:23]
	s_mul_i32 s26, s18, 0x180
	v_lshrrev_b32_e32 v57, 4, v0
	v_lshl_add_u64 v[24:25], v[24:25], 0, v[26:27]
	v_lshl_add_u64 v[22:23], v[22:23], 0, v[26:27]
	s_mulk_i32 s19, 0x60
	global_load_dword v69, v[22:23], off
	v_or_b32_e32 v22, s26, v57
	v_add_u32_e32 v22, s19, v22
	v_mov_b32_e32 v23, v55
	v_lshlrev_b64 v[22:23], 11, v[22:23]
	v_and_b32_e32 v72, 60, v54
	v_lshl_add_u64 v[22:23], s[22:23], 0, v[22:23]
	v_lshlrev_b32_e32 v54, 2, v72
	v_lshl_add_u64 v[66:67], v[22:23], 0, v[54:55]
	global_load_dwordx4 v[22:25], v[66:67], off
	s_mov_b32 s14, 0x10000
	v_add_co_u32_e32 v64, vcc, s14, v66
	s_mov_b32 s15, 0x20000
	s_nop 0
	v_addc_co_u32_e32 v65, vcc, 0, v67, vcc
	global_load_dwordx4 v[30:33], v[64:65], off
	v_add_co_u32_e32 v62, vcc, s15, v66
	v_or_b32_e32 v26, s20, v57
	s_nop 0
	v_addc_co_u32_e32 v63, vcc, 0, v67, vcc
	global_load_dwordx4 v[34:37], v[62:63], off
	v_lshlrev_b32_e32 v26, 9, v26
	v_lshl_add_u64 v[26:27], v[26:27], 2, s[12:13]
	v_lshl_add_u64 v[60:61], v[26:27], 0, v[54:55]
	v_add_co_u32_e32 v58, vcc, s14, v60
	global_load_dwordx4 v[38:41], v[60:61], off
	s_nop 0
	v_addc_co_u32_e32 v59, vcc, 0, v61, vcc
	global_load_dwordx4 v[42:45], v[58:59], off
	global_load_dwordx4 v[46:49], v[66:67], off offset:256
	global_load_dwordx4 v[50:53], v[64:65], off offset:256
	global_load_dwordx4 v[74:77], v[62:63], off offset:256
	global_load_dwordx4 v[78:81], v[60:61], off offset:256
	global_load_dwordx4 v[82:85], v[58:59], off offset:256
	global_load_dwordx4 v[86:89], v[66:67], off offset:512
	global_load_dwordx4 v[90:93], v[64:65], off offset:512
	v_lshrrev_b32_e32 v26, 8, v0
	v_mul_u32_u24_e32 v54, 48, v26
	global_load_dwordx4 v[26:29], v[62:63], off offset:512
	global_load_dwordx4 v[94:97], v[60:61], off offset:512
	v_or_b32_e32 v102, v54, v56
	v_and_b32_e32 v56, 48, v0
	s_movk_i32 s14, 0x90
	v_mad_u32_u24 v73, v68, s14, v56
	v_lshl_or_b32 v1, v1, 2, v54
	v_mul_lo_u32 v1, v1, s14
	v_lshl_add_u32 v1, v68, 1, v1
	s_movk_i32 s15, 0x180
	s_waitcnt vmcnt(13)
	v_cvt_f16_f32_e32 v22, v22
	v_cvt_f16_f32_e32 v25, v25
	v_cvt_pk_f16_f32 v23, v23, v24
	v_mul_u32_u24_e32 v24, 0x90, v57
	v_pack_b32_f16 v22, v22, v23
	v_alignbit_b32 v23, v25, v23, 16
	v_lshl_add_u32 v72, v72, 1, v24
	s_waitcnt vmcnt(12)
	v_cvt_f16_f32_e32 v25, v30
	v_cvt_f16_f32_e32 v30, v33
	v_cvt_pk_f16_f32 v31, v31, v32
	v_mad_u64_u32 v[56:57], s[12:13], v102, s14, v[56:57]
	v_pack_b32_f16 v24, v25, v31
	v_alignbit_b32 v25, v30, v31, 16
	s_waitcnt vmcnt(11)
	v_cvt_f16_f32_e32 v30, v34
	ds_write2st64_b64 v72, v[22:23], v[24:25] offset1:9
	s_waitcnt vmcnt(8)
	v_cvt_f16_f32_e32 v34, v46
	v_cvt_pk_f16_f32 v23, v35, v36
	v_cvt_f16_f32_e32 v35, v49
	v_cvt_pk_f16_f32 v36, v47, v48
	v_pack_b32_f16 v102, v34, v36
	s_waitcnt vmcnt(7)
	v_cvt_f16_f32_e32 v34, v50
	v_alignbit_b32 v103, v35, v36, 16
	v_cvt_f16_f32_e32 v35, v53
	v_cvt_pk_f16_f32 v36, v51, v52
	v_pack_b32_f16 v104, v34, v36
	s_waitcnt vmcnt(6)
	v_cvt_f16_f32_e32 v34, v74
	v_alignbit_b32 v105, v35, v36, 16
	v_cvt_f16_f32_e32 v35, v77
	v_cvt_pk_f16_f32 v36, v75, v76
	v_pack_b32_f16 v106, v34, v36
	s_waitcnt vmcnt(5)
	v_cvt_f16_f32_e32 v34, v78
	v_alignbit_b32 v107, v35, v36, 16
	v_cvt_f16_f32_e32 v35, v81
	v_cvt_pk_f16_f32 v36, v79, v80
	v_pack_b32_f16 v108, v34, v36
	s_waitcnt vmcnt(4)
	v_cvt_f16_f32_e32 v34, v82
	v_cvt_f16_f32_e32 v24, v37
	v_pack_b32_f16 v22, v30, v23
	v_cvt_f16_f32_e32 v25, v38
	v_cvt_f16_f32_e32 v30, v41
	v_alignbit_b32 v109, v35, v36, 16
	v_cvt_f16_f32_e32 v35, v85
	v_cvt_pk_f16_f32 v36, v83, v84
	v_cvt_pk_f16_f32 v31, v39, v40
	v_pack_b32_f16 v110, v34, v36
	s_waitcnt vmcnt(3)
	v_cvt_f16_f32_e32 v34, v86
	v_alignbit_b32 v23, v24, v23, 16
	v_pack_b32_f16 v24, v25, v31
	v_alignbit_b32 v25, v30, v31, 16
	v_cvt_f16_f32_e32 v30, v42
	v_cvt_f16_f32_e32 v31, v45
	v_alignbit_b32 v111, v35, v36, 16
	v_cvt_pk_f16_f32 v36, v87, v88
	v_cvt_pk_f16_f32 v32, v43, v44
	v_cvt_f16_f32_e32 v35, v89
	v_pack_b32_f16 v114, v34, v36
	s_waitcnt vmcnt(2)
	v_cvt_f16_f32_e32 v34, v90
	v_pack_b32_f16 v30, v30, v32
	v_alignbit_b32 v31, v31, v32, 16
	ds_write2st64_b64 v72, v[22:23], v[24:25] offset0:18 offset1:54
	global_load_dwordx4 v[22:25], v[58:59], off offset:512
	ds_write_b64 v72, v[30:31] offset:32256
	s_waitcnt lgkmcnt(0)
	s_barrier
	global_load_dwordx4 v[30:33], v[66:67], off offset:768
	global_load_dwordx4 v[98:101], v[64:65], off offset:768
	v_cvt_pk_f16_f32 v39, v91, v92
	v_alignbit_b32 v115, v35, v36, 16
	v_cvt_f16_f32_e32 v38, v93
	v_pack_b32_f16 v116, v34, v39
	ds_read_b128 v[34:37], v56
	s_waitcnt vmcnt(4)
	v_cvt_f16_f32_e32 v57, v26
	v_alignbit_b32 v117, v38, v39, 16
	ds_read_b128 v[38:41], v56 offset:2304
	ds_read_b128 v[46:49], v73 offset:27648
	ds_read_b128 v[50:53], v56 offset:4608
	ds_read_b128 v[74:77], v56 offset:64
	ds_read_b128 v[78:81], v73 offset:27712
	v_cvt_f16_f32_e32 v87, v29
	s_waitcnt lgkmcnt(3)
	v_mfma_f32_16x16x32_f16 v[34:37], v[34:37], v[46:49], 0
	v_cvt_pk_f16_f32 v86, v27, v28
	global_load_dwordx4 v[42:45], v[62:63], off offset:768
	ds_read_b128 v[26:29], v56 offset:2368
	v_mfma_f32_16x16x32_f16 v[82:85], v[38:41], v[46:49], 0
	v_pack_b32_f16 v118, v57, v86
	v_alignbit_b32 v119, v87, v86, 16
	ds_read_b128 v[86:89], v56 offset:4672
	s_waitcnt lgkmcnt(4)
	v_mfma_f32_16x16x32_f16 v[50:53], v[50:53], v[46:49], 0
	global_load_dwordx4 v[46:49], v[60:61], off offset:768
	ds_write2st64_b64 v72, v[102:103], v[104:105] offset0:27 offset1:36
	ds_write2st64_b64 v72, v[106:107], v[108:109] offset0:45 offset1:72
	ds_write_b64 v72, v[110:111] offset:41472
	s_waitcnt lgkmcnt(5)
	v_mfma_f32_16x16x32_f16 v[74:77], v[74:77], v[78:81], v[34:37]
	s_waitcnt vmcnt(5)
	v_cvt_f16_f32_e32 v57, v94
	v_cvt_f16_f32_e32 v90, v97
	v_cvt_pk_f16_f32 v91, v95, v96
	global_load_dwordx4 v[34:37], v[58:59], off offset:768
	s_waitcnt lgkmcnt(0)
	s_barrier
	global_load_dwordx4 v[38:41], v[66:67], off offset:1024
	v_pack_b32_f16 v120, v57, v91
	v_alignbit_b32 v121, v90, v91, 16
	global_load_dwordx4 v[90:93], v[64:65], off offset:1024
	v_mfma_f32_16x16x32_f16 v[50:53], v[86:89], v[78:81], v[50:53]
	global_load_dwordx4 v[86:89], v[62:63], off offset:1024
	s_load_dwordx2 s[12:13], s[0:1], 0x78
	s_waitcnt vmcnt(8)
	v_cvt_f16_f32_e32 v22, v22
	v_mfma_f32_16x16x32_f16 v[82:85], v[26:29], v[78:81], v[82:85]
	v_cvt_f16_f32_e32 v25, v25
	v_cvt_pk_f16_f32 v23, v23, v24
	v_pack_b32_f16 v122, v22, v23
	s_waitcnt vmcnt(7)
	v_cvt_f16_f32_e32 v26, v30
	v_cvt_pk_f16_f32 v57, v31, v32
	v_alignbit_b32 v123, v25, v23, 16
	ds_read_b128 v[22:25], v56 offset:13824
	ds_read_b128 v[78:81], v73 offset:36864
	v_cvt_f16_f32_e32 v125, v33
	s_waitcnt vmcnt(6)
	v_cvt_f16_f32_e32 v126, v98
	v_cvt_pk_f16_f32 v127, v99, v100
	v_cvt_f16_f32_e32 v128, v101
	ds_read_b128 v[94:97], v56 offset:13888
	ds_read_b128 v[98:101], v73 offset:36928
	ds_read_b128 v[30:33], v56 offset:16128
	ds_read_b128 v[102:105], v56 offset:16192
	ds_read_b128 v[106:109], v56 offset:18432
	ds_read_b128 v[110:113], v56 offset:18496
	ds_write2st64_b64 v72, v[114:115], v[116:117] offset1:9
	global_load_dwordx4 v[114:117], v[60:61], off offset:1024
	v_pack_b32_f16 v124, v26, v57
	global_load_dwordx4 v[26:29], v[58:59], off offset:1024
	s_waitcnt lgkmcnt(0)
	v_mfma_f32_16x16x32_f16 v[74:77], v[22:25], v[78:81], v[74:77]
	ds_write2st64_b64 v72, v[118:119], v[120:121] offset0:18 offset1:54
	s_waitcnt vmcnt(7)
	v_cvt_f16_f32_e32 v42, v42
	v_cvt_f16_f32_e32 v45, v45
	v_mfma_f32_16x16x32_f16 v[82:85], v[30:33], v[78:81], v[82:85]
	ds_write_b64 v72, v[122:123] offset:32256
	s_waitcnt lgkmcnt(0)
	s_barrier
	global_load_dwordx4 v[22:25], v[66:67], off offset:1280
	global_load_dwordx4 v[30:33], v[64:65], off offset:1280
	v_cvt_pk_f16_f32 v43, v43, v44
	v_alignbit_b32 v125, v125, v57, 16
	v_mfma_f32_16x16x32_f16 v[50:53], v[106:109], v[78:81], v[50:53]
	v_pack_b32_f16 v108, v42, v43
	v_alignbit_b32 v109, v45, v43, 16
	s_waitcnt vmcnt(7)
	v_cvt_f16_f32_e32 v34, v34
	v_cvt_pk_f16_f32 v35, v35, v36
	v_cvt_f16_f32_e32 v36, v37
	v_mfma_f32_16x16x32_f16 v[42:45], v[94:97], v[98:101], v[74:77]
	v_cvt_f16_f32_e32 v57, v46
	s_waitcnt vmcnt(6)
	v_cvt_f16_f32_e32 v37, v41
	v_pack_b32_f16 v106, v126, v127
	v_cvt_f16_f32_e32 v74, v49
	v_cvt_pk_f16_f32 v75, v47, v48
	v_mfma_f32_16x16x32_f16 v[46:49], v[102:105], v[98:101], v[82:85]
	v_pack_b32_f16 v104, v34, v35
	v_cvt_f16_f32_e32 v34, v38
	v_alignbit_b32 v105, v36, v35, 16
	v_cvt_pk_f16_f32 v35, v39, v40
	v_alignbit_b32 v119, v37, v35, 16
	v_pack_b32_f16 v118, v34, v35
	ds_read_b128 v[34:37], v56
	v_pack_b32_f16 v102, v57, v75
	v_alignbit_b32 v103, v74, v75, 16
	ds_read_b128 v[74:77], v56 offset:2304
	ds_read_b128 v[78:81], v73 offset:27648
	s_waitcnt vmcnt(5)
	v_cvt_f16_f32_e32 v38, v90
	v_cvt_f16_f32_e32 v40, v93
	v_mfma_f32_16x16x32_f16 v[50:53], v[110:113], v[98:101], v[50:53]
	v_cvt_pk_f16_f32 v39, v91, v92
	v_pack_b32_f16 v120, v38, v39
	v_alignbit_b32 v121, v40, v39, 16
	ds_read_b128 v[82:85], v56 offset:4608
	ds_read_b128 v[90:93], v56 offset:64
	ds_read_b128 v[94:97], v73 offset:27712
	s_waitcnt lgkmcnt(3)
	v_mfma_f32_16x16x32_f16 v[34:37], v[34:37], v[78:81], v[42:45]
	global_load_dwordx4 v[38:41], v[62:63], off offset:1280
	v_alignbit_b32 v107, v128, v127, 16
	ds_read_b128 v[98:101], v56 offset:2368
	s_waitcnt vmcnt(5)
	v_cvt_f16_f32_e32 v42, v86
	v_cvt_f16_f32_e32 v44, v89
	v_mfma_f32_16x16x32_f16 v[74:77], v[74:77], v[78:81], v[46:49]
	v_cvt_pk_f16_f32 v43, v87, v88
	v_pack_b32_f16 v122, v42, v43
	v_alignbit_b32 v123, v44, v43, 16
	s_waitcnt lgkmcnt(3)
	v_mfma_f32_16x16x32_f16 v[78:81], v[82:85], v[78:81], v[50:53]
	global_load_dwordx4 v[42:45], v[58:59], off offset:1280
	ds_read_b128 v[86:89], v56 offset:4672
	ds_write2st64_b64 v72, v[124:125], v[106:107] offset0:27 offset1:36
	global_load_dwordx4 v[50:53], v[60:61], off offset:1280
	ds_write2st64_b64 v72, v[108:109], v[102:103] offset0:45 offset1:72
	ds_write_b64 v72, v[104:105] offset:41472
	s_waitcnt lgkmcnt(0)
	s_barrier
	global_load_dwordx4 v[46:49], v[66:67], off offset:1536
	global_load_dwordx4 v[82:85], v[64:65], off offset:1536
	v_mfma_f32_16x16x32_f16 v[78:81], v[86:89], v[94:97], v[78:81]
	ds_read_b128 v[86:89], v73 offset:36864
	s_waitcnt vmcnt(8)
	v_cvt_f16_f32_e32 v57, v114
	v_mfma_f32_16x16x32_f16 v[34:37], v[90:93], v[94:97], v[34:37]
	s_waitcnt vmcnt(7)
	v_cvt_f16_f32_e32 v26, v26
	v_cvt_f16_f32_e32 v29, v29
	v_cvt_pk_f16_f32 v27, v27, v28
	v_cvt_f16_f32_e32 v91, v117
	v_pack_b32_f16 v126, v26, v27
	v_alignbit_b32 v127, v29, v27, 16
	ds_read_b128 v[26:29], v56 offset:13824
	v_cvt_pk_f16_f32 v90, v115, v116
	v_pack_b32_f16 v124, v57, v90
	v_mfma_f32_16x16x32_f16 v[74:77], v[98:101], v[94:97], v[74:77]
	v_alignbit_b32 v125, v91, v90, 16
	s_waitcnt vmcnt(5)
	v_cvt_f16_f32_e32 v130, v30
	v_cvt_pk_f16_f32 v131, v31, v32
	v_cvt_f16_f32_e32 v132, v33
	ds_read_b128 v[90:93], v56 offset:13888
	global_load_dwordx4 v[94:97], v[62:63], off offset:1536
	ds_read_b128 v[98:101], v73 offset:36928
	s_waitcnt lgkmcnt(2)
	v_mfma_f32_16x16x32_f16 v[26:29], v[26:29], v[86:89], v[34:37]
	ds_read_b128 v[30:33], v56 offset:16128
	ds_read_b128 v[102:105], v56 offset:16192
	ds_read_b128 v[106:109], v56 offset:18432
	ds_read_b128 v[110:113], v56 offset:18496
	global_load_dwordx4 v[114:117], v[60:61], off offset:1536
	global_load_dwordx4 v[34:37], v[58:59], off offset:1536
	v_cvt_f16_f32_e32 v57, v22
	v_cvt_pk_f16_f32 v128, v23, v24
	v_cvt_f16_f32_e32 v129, v25
	ds_write2st64_b64 v72, v[118:119], v[120:121] offset1:9
	ds_write2st64_b64 v72, v[122:123], v[124:125] offset0:18 offset1:54
	ds_write_b64 v72, v[126:127] offset:32256
	s_waitcnt lgkmcnt(0)
	s_barrier
	global_load_dwordx4 v[22:25], v[66:67], off offset:1792
	v_mfma_f32_16x16x32_f16 v[74:77], v[30:33], v[86:89], v[74:77]
	global_load_dwordx4 v[30:33], v[64:65], off offset:1792
	v_pack_b32_f16 v118, v57, v128
	v_alignbit_b32 v119, v129, v128, 16
	v_mfma_f32_16x16x32_f16 v[64:67], v[106:109], v[86:89], v[78:81]
	v_pack_b32_f16 v120, v130, v131
	v_alignbit_b32 v121, v132, v131, 16
	s_waitcnt vmcnt(9)
	v_cvt_f16_f32_e32 v38, v38
	v_cvt_f16_f32_e32 v41, v41
	v_cvt_pk_f16_f32 v39, v39, v40
	v_mfma_f32_16x16x32_f16 v[78:81], v[90:93], v[98:101], v[26:29]
	v_pack_b32_f16 v106, v38, v39
	v_alignbit_b32 v107, v41, v39, 16
	s_waitcnt vmcnt(8)
	v_cvt_f16_f32_e32 v38, v42
	v_cvt_f16_f32_e32 v40, v45
	v_cvt_pk_f16_f32 v39, v43, v44
	s_waitcnt vmcnt(7)
	v_cvt_f16_f32_e32 v26, v50
	v_cvt_f16_f32_e32 v27, v53
	v_cvt_pk_f16_f32 v28, v51, v52
	v_mfma_f32_16x16x32_f16 v[50:53], v[102:105], v[98:101], v[74:77]
	v_pack_b32_f16 v102, v26, v28
	v_alignbit_b32 v103, v27, v28, 16
	global_load_dwordx4 v[26:29], v[62:63], off offset:1792
	v_pack_b32_f16 v104, v38, v39
	s_waitcnt vmcnt(7)
	v_cvt_f16_f32_e32 v38, v46
	v_alignbit_b32 v105, v40, v39, 16
	v_cvt_f16_f32_e32 v39, v49
	s_waitcnt vmcnt(6)
	v_cvt_f16_f32_e32 v44, v82
	v_cvt_pk_f16_f32 v40, v47, v48
	v_cvt_pk_f16_f32 v48, v83, v84
	v_pack_b32_f16 v38, v38, v40
	v_alignbit_b32 v39, v39, v40, 16
	ds_read_b128 v[40:43], v56
	v_pack_b32_f16 v108, v44, v48
	v_cvt_f16_f32_e32 v49, v85
	ds_read_b128 v[44:47], v56 offset:2304
	ds_read_b128 v[74:77], v73 offset:27648
	ds_read_b128 v[82:85], v56 offset:4608
	global_load_dwordx4 v[60:63], v[60:61], off offset:1792
	v_mfma_f32_16x16x32_f16 v[64:67], v[110:113], v[98:101], v[64:67]
	ds_read_b128 v[86:89], v56 offset:64
	ds_read_b128 v[90:93], v73 offset:27712
	global_load_dwordx4 v[98:101], v[58:59], off offset:1792
	v_alignbit_b32 v109, v49, v48, 16
	s_waitcnt lgkmcnt(3)
	v_mfma_f32_16x16x32_f16 v[40:43], v[40:43], v[74:77], v[78:81]
	s_waitcnt vmcnt(7)
	v_cvt_pk_f16_f32 v57, v95, v96
	s_nop 0
	ds_read_b128 v[78:81], v56 offset:2368
	v_mfma_f32_16x16x32_f16 v[44:47], v[44:47], v[74:77], v[50:53]
	s_waitcnt vmcnt(6)
	v_cvt_f16_f32_e32 v59, v117
	s_waitcnt vmcnt(5)
	v_cvt_f16_f32_e32 v34, v34
	ds_read_b128 v[48:51], v56 offset:4672
	v_cvt_f16_f32_e32 v52, v94
	v_cvt_f16_f32_e32 v53, v97
	v_cvt_f16_f32_e32 v37, v37
	v_cvt_pk_f16_f32 v35, v35, v36
	s_waitcnt lgkmcnt(4)
	v_mfma_f32_16x16x32_f16 v[64:67], v[82:85], v[74:77], v[64:67]
	v_pack_b32_f16 v52, v52, v57
	v_alignbit_b32 v53, v53, v57, 16
	v_cvt_f16_f32_e32 v57, v114
	s_waitcnt lgkmcnt(2)
	v_mfma_f32_16x16x32_f16 v[40:43], v[86:89], v[90:93], v[40:43]
	ds_write2st64_b64 v72, v[118:119], v[120:121] offset0:27 offset1:36
	ds_write2st64_b64 v72, v[106:107], v[102:103] offset0:45 offset1:72
	ds_write_b64 v72, v[104:105] offset:41472
	v_pack_b32_f16 v86, v34, v35
	v_alignbit_b32 v87, v37, v35, 16
	s_waitcnt lgkmcnt(0)
	s_barrier
	ds_read_b128 v[34:37], v56 offset:13824
	v_cvt_pk_f16_f32 v74, v115, v116
	v_pack_b32_f16 v58, v57, v74
	v_alignbit_b32 v59, v59, v74, 16
	v_mfma_f32_16x16x32_f16 v[48:51], v[48:51], v[90:93], v[64:67]
	s_nop 2
	ds_read_b128 v[64:67], v56 offset:16128
	ds_read_b128 v[74:77], v73 offset:36864
	s_waitcnt vmcnt(4)
	v_cvt_f16_f32_e32 v57, v22
	v_cvt_pk_f16_f32 v89, v23, v24
	v_mfma_f32_16x16x32_f16 v[44:47], v[78:81], v[90:93], v[44:47]
	v_cvt_f16_f32_e32 v90, v25
	ds_read_b128 v[22:25], v56 offset:18432
	ds_read_b128 v[78:81], v56 offset:13888
	ds_read_b128 v[82:85], v73 offset:36928
	s_waitcnt vmcnt(3)
	v_cvt_f16_f32_e32 v30, v30
	s_waitcnt lgkmcnt(3)
	v_mfma_f32_16x16x32_f16 v[34:37], v[34:37], v[74:77], v[40:43]
	v_cvt_f16_f32_e32 v33, v33
	v_cvt_pk_f16_f32 v31, v31, v32
	v_pack_b32_f16 v88, v57, v89
	ds_read_b128 v[40:43], v56 offset:16192
	v_mfma_f32_16x16x32_f16 v[44:47], v[64:67], v[74:77], v[44:47]
	ds_read_b128 v[64:67], v56 offset:18496
	v_alignbit_b32 v89, v90, v89, 16
	v_pack_b32_f16 v90, v30, v31
	s_waitcnt lgkmcnt(4)
	v_mfma_f32_16x16x32_f16 v[22:25], v[22:25], v[74:77], v[48:51]
	v_alignbit_b32 v91, v33, v31, 16
	ds_write2st64_b64 v72, v[38:39], v[108:109] offset1:9
	ds_write2st64_b64 v72, v[52:53], v[58:59] offset0:18 offset1:54
	ds_write_b64 v72, v[86:87] offset:32256
	s_waitcnt lgkmcnt(0)
	v_mfma_f32_16x16x32_f16 v[30:33], v[78:81], v[82:85], v[34:37]
	s_barrier
	s_waitcnt vmcnt(2)
	v_cvt_f16_f32_e32 v57, v26
	ds_read_b128 v[34:37], v56
	v_mfma_f32_16x16x32_f16 v[38:41], v[40:43], v[82:85], v[44:47]
	s_nop 2
	ds_read_b128 v[42:45], v56 offset:2304
	ds_read_b128 v[46:49], v73 offset:27648
	v_cvt_pk_f16_f32 v58, v27, v28
	v_cvt_f16_f32_e32 v59, v29
	v_mfma_f32_16x16x32_f16 v[22:25], v[64:67], v[82:85], v[22:25]
	ds_read_b128 v[50:53], v56 offset:4608
	ds_read_b128 v[64:67], v56 offset:64
	ds_read_b128 v[74:77], v73 offset:27712
	ds_read_b128 v[26:29], v56 offset:2368
	s_waitcnt lgkmcnt(4)
	v_mfma_f32_16x16x32_f16 v[30:33], v[34:37], v[46:49], v[30:33]
	v_mfma_f32_16x16x32_f16 v[34:37], v[42:45], v[46:49], v[38:41]
	s_waitcnt vmcnt(1)
	v_cvt_f16_f32_e32 v44, v60
	v_cvt_f16_f32_e32 v45, v63
	v_pack_b32_f16 v42, v57, v58
	s_waitcnt lgkmcnt(3)
	v_mfma_f32_16x16x32_f16 v[22:25], v[50:53], v[46:49], v[22:25]
	v_cvt_pk_f16_f32 v46, v61, v62
	ds_read_b128 v[38:41], v56 offset:4672
	v_pack_b32_f16 v44, v44, v46
	v_alignbit_b32 v45, v45, v46, 16
	s_waitcnt vmcnt(0)
	v_cvt_f16_f32_e32 v46, v98
	s_waitcnt lgkmcnt(1)
	v_mfma_f32_16x16x32_f16 v[26:29], v[26:29], v[74:77], v[34:37]
	v_alignbit_b32 v43, v59, v58, 16
	ds_write2st64_b64 v72, v[88:89], v[90:91] offset0:27 offset1:36
	ds_write2st64_b64 v72, v[42:43], v[44:45] offset0:45 offset1:72
	v_cvt_f16_f32_e32 v35, v101
	v_cvt_pk_f16_f32 v36, v99, v100
	v_pack_b32_f16 v34, v46, v36
	v_mfma_f32_16x16x32_f16 v[30:33], v[64:67], v[74:77], v[30:33]
	v_alignbit_b32 v35, v35, v36, 16
	ds_write_b64 v72, v[34:35] offset:41472
	s_waitcnt lgkmcnt(0)
	s_barrier
	ds_read_b128 v[34:37], v56 offset:13824
	v_mfma_f32_16x16x32_f16 v[22:25], v[38:41], v[74:77], v[22:25]
	ds_read_b128 v[38:41], v73 offset:36864
	ds_read_b128 v[42:45], v56 offset:13888
	ds_read_b128 v[46:49], v73 offset:36928
	s_waitcnt lgkmcnt(2)
	v_mfma_f32_16x16x32_f16 v[30:33], v[34:37], v[38:41], v[30:33]
	ds_read_b128 v[34:37], v56 offset:16128
	ds_read_b128 v[50:53], v56 offset:16192
	s_waitcnt lgkmcnt(2)
	v_mfma_f32_16x16x32_f16 v[30:33], v[42:45], v[46:49], v[30:33]
	s_waitcnt lgkmcnt(1)
	v_mfma_f32_16x16x32_f16 v[26:29], v[34:37], v[38:41], v[26:29]
	ds_read_b128 v[34:37], v56 offset:18432
	ds_read_b128 v[56:59], v56 offset:18496
	s_waitcnt vmcnt(0)
	s_waitcnt lgkmcnt(0)
	s_nop 2
	v_add_f32_e32 v2, v30, v69
	v_mfma_f32_16x16x32_f16 v[26:29], v[50:53], v[46:49], v[26:29]
	v_cvt_f16_f32_e32 v2, v2
	v_add_f32_e32 v3, v31, v69
	v_cvt_f16_f32_e32 v3, v3
	v_mfma_f32_16x16x32_f16 v[22:25], v[34:37], v[38:41], v[22:25]
	v_add_f32_e32 v4, v32, v69
	v_cvt_f16_f32_e32 v4, v4
	v_add_f32_e32 v5, v33, v69
	v_cvt_f16_f32_e32 v5, v5
	s_barrier
	ds_write_b16 v1, v2
	ds_write_b16 v1, v3 offset:144
	ds_write_b16 v1, v4 offset:288
	ds_write_b16 v1, v5 offset:432
	v_add_f32_e32 v2, v26, v69
	v_mfma_f32_16x16x32_f16 v[22:25], v[56:59], v[46:49], v[22:25]
	v_cvt_f16_f32_e32 v2, v2
	v_add_f32_e32 v3, v27, v69
	v_cvt_f16_f32_e32 v3, v3
	v_add_f32_e32 v4, v28, v69
	v_cvt_f16_f32_e32 v4, v4
	v_add_f32_e32 v5, v29, v69
	v_cvt_f16_f32_e32 v5, v5
	ds_write_b16 v1, v2 offset:2304
	ds_write_b16 v1, v3 offset:2448
	ds_write_b16 v1, v4 offset:2592
	ds_write_b16 v1, v5 offset:2736
	v_add_f32_e32 v2, v22, v69
	v_cvt_f16_f32_e32 v2, v2
	v_add_f32_e32 v3, v23, v69
	v_cvt_f16_f32_e32 v3, v3
	v_add_f32_e32 v4, v24, v69
	v_cvt_f16_f32_e32 v4, v4
	v_add_f32_e32 v5, v25, v69
	v_cvt_f16_f32_e32 v5, v5
	ds_write_b16 v1, v2 offset:4608
	ds_write_b16 v1, v3 offset:4752
	ds_write_b16 v1, v4 offset:4896
	ds_write_b16 v1, v5 offset:5040
	v_and_b32_e32 v2, 7, v0
	v_mul_u32_u24_e32 v10, 12, v2
	v_mul_u32_u24_e32 v2, 0x360, v2
	v_lshrrev_b32_e32 v1, 3, v0
	v_lshlrev_b32_e32 v2, 1, v2
	v_lshl_add_u32 v3, v1, 1, v2
	s_waitcnt lgkmcnt(0)
	s_barrier
	ds_read_u16 v2, v3
	ds_read_u16 v4, v3 offset:144
	ds_read_u16 v5, v3 offset:288
	ds_read_u16 v6, v3 offset:432
	ds_read_u16 v7, v3 offset:576
	ds_read_u16 v8, v3 offset:720
	ds_read_u16 v9, v3 offset:864
	ds_read_u16 v11, v3 offset:1008
	ds_read_u16 v12, v3 offset:1152
	ds_read_u16 v13, v3 offset:1296
	ds_read_u16 v14, v3 offset:1440
	ds_read_u16 v15, v3 offset:1584
	v_lshl_or_b32 v1, s18, 9, v1
	s_waitcnt lgkmcnt(10)
	v_lshl_or_b32 v2, v4, 16, v2
	s_waitcnt lgkmcnt(6)
	v_lshl_or_b32 v4, v8, 16, v7
	v_or_b32_e32 v1, s20, v1
	v_mov_b32_e32 v8, s19
	v_mad_u32_u24 v54, v1, s15, v8
	v_lshl_or_b32 v3, v6, 16, v5
	s_waitcnt lgkmcnt(4)
	v_lshl_or_b32 v5, v11, 16, v9
	v_lshl_add_u64 v[8:9], v[54:55], 1, s[12:13]
	v_lshlrev_b32_e32 v54, 1, v10
	v_lshl_add_u64 v[8:9], v[8:9], 0, v[54:55]
	s_waitcnt lgkmcnt(2)
	v_lshl_or_b32 v6, v13, 16, v12
	s_waitcnt lgkmcnt(0)
	v_lshl_or_b32 v7, v15, 16, v14
	global_store_dwordx4 v[8:9], v[2:5], off
	global_store_dwordx2 v[8:9], v[6:7], off offset:16
	s_mov_b64 s[12:13], 0
